# baseline (speedup 1.0000x reference)
.Lmy_proj_noprio:
	s_load_dwordx4 s[4:7], s[0:1], 0x20
	s_load_dwordx2 s[12:13], s[0:1], 0x30
	v_and_b32_e32 v73, 63, v0
	v_and_b32_e32 v1, 31, v0
	v_lshrrev_b32_e32 v76, 6, v0
	v_bfe_u32 v77, v0, 5, 1
	v_or_b32_e32 v45, 0x200, v0
	v_or_b32_e32 v46, 0x600, v0
	v_or_b32_e32 v47, 0xa00, v0
	v_or_b32_e32 v48, 0xe00, v0
	v_lshlrev_b32_e32 v34, 15, v76
	v_mov_b32_e32 v35, v71
	v_lshl_add_u64 v[34:35], s[8:9], 0, v[34:35]
	v_lshlrev_b32_e32 v36, 4, v73
	v_mov_b32_e32 v37, v71
	v_lshl_add_u64 v[68:69], v[34:35], 0, v[36:37]
	s_movk_i32 s0, 0x5000
	v_add_co_u32_e32 v38, vcc, s0, v68
	s_movk_i32 s0, 0x4000
	s_nop 0
	v_addc_co_u32_e32 v39, vcc, 0, v69, vcc
	global_load_dwordx4 v[34:37], v[68:69], off
	global_load_dwordx4 v[78:81], v[38:39], off offset:-4096
	v_add_co_u32_e32 v40, vcc, s0, v68
	s_nop 1
	v_addc_co_u32_e32 v41, vcc, 0, v69, vcc
	global_load_dwordx4 v[82:85], v[68:69], off offset:1024
	global_load_dwordx4 v[86:89], v[40:41], off offset:1024
	global_load_dwordx4 v[90:93], v[68:69], off offset:2048
	global_load_dwordx4 v[94:97], v[40:41], off offset:2048
	global_load_dwordx4 v[98:101], v[68:69], off offset:3072
	global_load_dwordx4 v[102:105], v[40:41], off offset:3072
	v_add_co_u32_e32 v74, vcc, s14, v68
	s_movk_i32 s0, 0x1000
	s_nop 0
	v_addc_co_u32_e32 v75, vcc, 0, v69, vcc
	global_load_dwordx4 v[106:109], v[74:75], off offset:-4096
	global_load_dwordx4 v[110:113], v[38:39], off
	v_add_co_u32_e32 v40, vcc, s0, v68
	s_nop 1
	v_addc_co_u32_e32 v41, vcc, 0, v69, vcc
	global_load_dwordx4 v[114:117], v[40:41], off offset:1024
	global_load_dwordx4 v[118:121], v[38:39], off offset:1024
	global_load_dwordx4 v[122:125], v[40:41], off offset:2048
	global_load_dwordx4 v[126:129], v[38:39], off offset:2048
	global_load_dwordx4 v[130:133], v[40:41], off offset:3072
	global_load_dwordx4 v[134:137], v[38:39], off offset:3072
	v_lshlrev_b32_e32 v38, 3, v0
	v_and_b32_e32 v38, 0x1f8, v38
	v_add_u32_e32 v38, 0, v38
	s_movk_i32 s0, 0x210
	s_waitcnt vmcnt(17)
	v_cvt_pk_f16_f32 v29, v28, v29
	v_cvt_pk_f16_f32 v28, v26, v27
	v_mad_u32_u24 v26, v76, s0, v38
	ds_write_b64 v26, v[28:29]
	v_lshrrev_b32_e32 v26, 6, v45
	v_cvt_pk_f16_f32 v5, v4, v5
	v_cvt_pk_f16_f32 v4, v2, v3
	v_mad_u32_u24 v2, v26, s0, v38
	ds_write_b64 v2, v[4:5]
	v_lshrrev_b32_e32 v4, 6, v42
	v_cvt_pk_f16_f32 v3, v8, v9
	v_cvt_pk_f16_f32 v2, v6, v7
	v_mad_u32_u24 v4, v4, s0, v38
	ds_write_b64 v4, v[2:3]
	v_lshrrev_b32_e32 v4, 6, v46
	v_cvt_pk_f16_f32 v3, v12, v13
	v_cvt_pk_f16_f32 v2, v10, v11
	v_mad_u32_u24 v4, v4, s0, v38
	ds_write_b64 v4, v[2:3]
	v_lshrrev_b32_e32 v4, 6, v43
	v_cvt_pk_f16_f32 v3, v16, v17
	v_cvt_pk_f16_f32 v2, v14, v15
	v_mad_u32_u24 v4, v4, s0, v38
	ds_write_b64 v4, v[2:3]
	v_lshrrev_b32_e32 v4, 6, v47
	v_cvt_pk_f16_f32 v3, v20, v21
	v_cvt_pk_f16_f32 v2, v18, v19
	v_mad_u32_u24 v4, v4, s0, v38
	ds_write_b64 v4, v[2:3]
	v_lshrrev_b32_e32 v4, 6, v44
	v_cvt_pk_f16_f32 v3, v24, v25
	v_cvt_pk_f16_f32 v2, v22, v23
	v_mad_u32_u24 v4, v4, s0, v38
	ds_write_b64 v4, v[2:3]
	v_lshrrev_b32_e32 v4, 6, v48
	s_waitcnt vmcnt(16)
	v_cvt_pk_f16_f32 v3, v32, v33
	v_cvt_pk_f16_f32 v2, v30, v31
	v_mad_u32_u24 v4, v4, s0, v38
	ds_write_b64 v4, v[2:3]
	v_mul_u32_u24_e32 v2, 0x210, v1
	v_lshlrev_b32_e32 v66, 4, v77
	v_add3_u32 v67, 0, v2, v66
	s_waitcnt lgkmcnt(0)
	s_barrier
	ds_read_b128 v[2:5], v67
	ds_read_b128 v[138:141], v67 offset:32
	ds_read_b128 v[6:9], v67 offset:16896
	ds_read_b128 v[142:145], v67 offset:16928
	s_movk_i32 s0, 0x7000
	v_add_co_u32_e32 v166, vcc, s0, v68
	s_waitcnt vmcnt(15) lgkmcnt(3)
	v_mfma_f32_32x32x16_f16 v[50:65], v[34:37], v[2:5], 0
	v_addc_co_u32_e32 v167, vcc, 0, v69, vcc
	global_load_dwordx4 v[146:149], v[74:75], off
	global_load_dwordx4 v[150:153], v[166:167], off offset:-4096
	ds_read_b128 v[154:157], v67 offset:64
	ds_read_b128 v[158:161], v67 offset:16960
	v_add_co_u32_e32 v168, vcc, s3, v68
	s_waitcnt lgkmcnt(3)
	v_mfma_f32_32x32x16_f16 v[34:49], v[34:37], v[6:9], 0
	v_addc_co_u32_e32 v169, vcc, 0, v69, vcc
	s_waitcnt vmcnt(16)
	v_mfma_f32_32x32x16_f16 v[18:33], v[78:81], v[2:5], 0
	v_mfma_f32_32x32x16_f16 v[2:17], v[78:81], v[6:9], 0
	s_waitcnt vmcnt(15)
	v_mfma_f32_32x32x16_f16 v[50:65], v[82:85], v[138:141], v[50:65]
	s_waitcnt lgkmcnt(2)
	v_mfma_f32_32x32x16_f16 v[34:49], v[82:85], v[142:145], v[34:49]
	global_load_dwordx4 v[78:81], v[74:75], off offset:1024
	global_load_dwordx4 v[82:85], v[168:169], off offset:1024
	s_waitcnt vmcnt(16)
	v_mfma_f32_32x32x16_f16 v[2:17], v[86:89], v[142:145], v[2:17]
	v_mfma_f32_32x32x16_f16 v[18:33], v[86:89], v[138:141], v[18:33]
	ds_read_b128 v[138:141], v67 offset:96
	ds_read_b128 v[162:165], v67 offset:16992
	s_waitcnt vmcnt(15) lgkmcnt(3)
	v_mfma_f32_32x32x16_f16 v[50:65], v[90:93], v[154:157], v[50:65]
	s_waitcnt lgkmcnt(2)
	v_mfma_f32_32x32x16_f16 v[34:49], v[90:93], v[158:161], v[34:49]
	global_load_dwordx4 v[86:89], v[74:75], off offset:2048
	global_load_dwordx4 v[90:93], v[168:169], off offset:2048
	s_waitcnt vmcnt(16)
	v_mfma_f32_32x32x16_f16 v[2:17], v[94:97], v[158:161], v[2:17]
	v_mfma_f32_32x32x16_f16 v[18:33], v[94:97], v[154:157], v[18:33]
	ds_read_b128 v[142:145], v67 offset:128
	ds_read_b128 v[154:157], v67 offset:17024
	s_waitcnt vmcnt(15) lgkmcnt(3)
	v_mfma_f32_32x32x16_f16 v[50:65], v[98:101], v[138:141], v[50:65]
	s_waitcnt lgkmcnt(2)
	v_mfma_f32_32x32x16_f16 v[34:49], v[98:101], v[162:165], v[34:49]
	global_load_dwordx4 v[94:97], v[74:75], off offset:3072
	global_load_dwordx4 v[98:101], v[168:169], off offset:3072
	s_waitcnt vmcnt(16)
	v_mfma_f32_32x32x16_f16 v[2:17], v[102:105], v[162:165], v[2:17]
	v_mfma_f32_32x32x16_f16 v[18:33], v[102:105], v[138:141], v[18:33]
	ds_read_b128 v[138:141], v67 offset:160
	ds_read_b128 v[158:161], v67 offset:17056
	s_movk_i32 s0, 0x3000
	v_add_co_u32_e32 v68, vcc, s0, v68
	s_waitcnt vmcnt(15) lgkmcnt(3)
	v_mfma_f32_32x32x16_f16 v[50:65], v[106:109], v[142:145], v[50:65]
	v_addc_co_u32_e32 v69, vcc, 0, v69, vcc
	s_waitcnt lgkmcnt(2)
	v_mfma_f32_32x32x16_f16 v[34:49], v[106:109], v[154:157], v[34:49]
	global_load_dwordx4 v[102:105], v[68:69], off
	global_load_dwordx4 v[106:109], v[166:167], off
	s_waitcnt vmcnt(16)
	v_mfma_f32_32x32x16_f16 v[2:17], v[110:113], v[154:157], v[2:17]
	v_mfma_f32_32x32x16_f16 v[18:33], v[110:113], v[142:145], v[18:33]
	ds_read_b128 v[142:145], v67 offset:192
	ds_read_b128 v[162:165], v67 offset:17088
	s_waitcnt vmcnt(15) lgkmcnt(3)
	v_mfma_f32_32x32x16_f16 v[50:65], v[114:117], v[138:141], v[50:65]
	s_waitcnt lgkmcnt(2)
	v_mfma_f32_32x32x16_f16 v[34:49], v[114:117], v[158:161], v[34:49]
	global_load_dwordx4 v[110:113], v[68:69], off offset:1024
	global_load_dwordx4 v[114:117], v[166:167], off offset:1024
	s_waitcnt vmcnt(16)
	v_mfma_f32_32x32x16_f16 v[2:17], v[118:121], v[158:161], v[2:17]
	v_mfma_f32_32x32x16_f16 v[18:33], v[118:121], v[138:141], v[18:33]
	ds_read_b128 v[138:141], v67 offset:224
	ds_read_b128 v[154:157], v67 offset:17120
	s_waitcnt vmcnt(15) lgkmcnt(3)
	v_mfma_f32_32x32x16_f16 v[50:65], v[122:125], v[142:145], v[50:65]
	s_waitcnt lgkmcnt(2)
	v_mfma_f32_32x32x16_f16 v[34:49], v[122:125], v[162:165], v[34:49]
	global_load_dwordx4 v[118:121], v[68:69], off offset:2048
	global_load_dwordx4 v[122:125], v[166:167], off offset:2048
	s_waitcnt vmcnt(16)
	v_mfma_f32_32x32x16_f16 v[2:17], v[126:129], v[162:165], v[2:17]
	v_mfma_f32_32x32x16_f16 v[18:33], v[126:129], v[142:145], v[18:33]
	ds_read_b128 v[142:145], v67 offset:256
	ds_read_b128 v[158:161], v67 offset:17152
	s_waitcnt vmcnt(15) lgkmcnt(3)
	v_mfma_f32_32x32x16_f16 v[50:65], v[130:133], v[138:141], v[50:65]
	s_waitcnt lgkmcnt(2)
	v_mfma_f32_32x32x16_f16 v[34:49], v[130:133], v[154:157], v[34:49]
	global_load_dwordx4 v[126:129], v[68:69], off offset:3072
	global_load_dwordx4 v[130:133], v[166:167], off offset:3072
	s_waitcnt vmcnt(16)
	v_mfma_f32_32x32x16_f16 v[2:17], v[134:137], v[154:157], v[2:17]
	v_mfma_f32_32x32x16_f16 v[18:33], v[134:137], v[138:141], v[18:33]
	ds_read_b128 v[138:141], v67 offset:288
	ds_read_b128 v[162:165], v67 offset:17184
	s_waitcnt vmcnt(14) lgkmcnt(2)
	v_mfma_f32_32x32x16_f16 v[2:17], v[150:153], v[158:161], v[2:17]
	v_mfma_f32_32x32x16_f16 v[50:65], v[146:149], v[142:145], v[50:65]
	v_mfma_f32_32x32x16_f16 v[18:33], v[150:153], v[142:145], v[18:33]
	ds_read_b128 v[134:137], v67 offset:320
	ds_read_b128 v[142:145], v67 offset:17216
	v_mfma_f32_32x32x16_f16 v[34:49], v[146:149], v[158:161], v[34:49]
	s_waitcnt vmcnt(12) lgkmcnt(2)
	v_mfma_f32_32x32x16_f16 v[2:17], v[82:85], v[162:165], v[2:17]
	v_mfma_f32_32x32x16_f16 v[50:65], v[78:81], v[138:141], v[50:65]
	v_mfma_f32_32x32x16_f16 v[34:49], v[78:81], v[162:165], v[34:49]
	v_mfma_f32_32x32x16_f16 v[18:33], v[82:85], v[138:141], v[18:33]
	ds_read_b128 v[78:81], v67 offset:352
	ds_read_b128 v[138:141], v67 offset:17248
	s_waitcnt vmcnt(10) lgkmcnt(2)
	v_mfma_f32_32x32x16_f16 v[2:17], v[90:93], v[142:145], v[2:17]
	v_mfma_f32_32x32x16_f16 v[50:65], v[86:89], v[134:137], v[50:65]
	v_mfma_f32_32x32x16_f16 v[34:49], v[86:89], v[142:145], v[34:49]
	ds_read_b128 v[82:85], v67 offset:384
	ds_read_b128 v[86:89], v67 offset:17280
	v_mfma_f32_32x32x16_f16 v[18:33], v[90:93], v[134:137], v[18:33]
	s_waitcnt vmcnt(8) lgkmcnt(2)
	v_mfma_f32_32x32x16_f16 v[2:17], v[98:101], v[138:141], v[2:17]
	v_mfma_f32_32x32x16_f16 v[50:65], v[94:97], v[78:81], v[50:65]
	v_mfma_f32_32x32x16_f16 v[18:33], v[98:101], v[78:81], v[18:33]
	ds_read_b128 v[78:81], v67 offset:416
	ds_read_b128 v[90:93], v67 offset:17312
	v_mfma_f32_32x32x16_f16 v[34:49], v[94:97], v[138:141], v[34:49]
	s_waitcnt vmcnt(6) lgkmcnt(2)
	v_mfma_f32_32x32x16_f16 v[2:17], v[106:109], v[86:89], v[2:17]
	v_mfma_f32_32x32x16_f16 v[50:65], v[102:105], v[82:85], v[50:65]
	v_mfma_f32_32x32x16_f16 v[18:33], v[106:109], v[82:85], v[18:33]
	ds_read_b128 v[82:85], v67 offset:448
	ds_read_b128 v[94:97], v67 offset:17344
	v_mfma_f32_32x32x16_f16 v[34:49], v[102:105], v[86:89], v[34:49]
	s_waitcnt vmcnt(4) lgkmcnt(2)
	v_mfma_f32_32x32x16_f16 v[2:17], v[114:117], v[90:93], v[2:17]
	v_mfma_f32_32x32x16_f16 v[50:65], v[110:113], v[78:81], v[50:65]
	v_mfma_f32_32x32x16_f16 v[18:33], v[114:117], v[78:81], v[18:33]
	ds_read_b128 v[78:81], v67 offset:480
	ds_read_b128 v[86:89], v67 offset:17376
	v_mfma_f32_32x32x16_f16 v[34:49], v[110:113], v[90:93], v[34:49]
	s_waitcnt vmcnt(2) lgkmcnt(2)
	v_mfma_f32_32x32x16_f16 v[2:17], v[122:125], v[94:97], v[2:17]
	v_mfma_f32_32x32x16_f16 v[50:65], v[118:121], v[82:85], v[50:65]
	v_mfma_f32_32x32x16_f16 v[34:49], v[118:121], v[94:97], v[34:49]
	v_mfma_f32_32x32x16_f16 v[18:33], v[122:125], v[82:85], v[18:33]
	s_waitcnt vmcnt(0) lgkmcnt(0)
	v_mfma_f32_32x32x16_f16 v[2:17], v[130:133], v[86:89], v[2:17]
	v_mfma_f32_32x32x16_f16 v[50:65], v[126:129], v[78:81], v[50:65]
	v_mfma_f32_32x32x16_f16 v[34:49], v[126:129], v[86:89], v[34:49]
	v_mfma_f32_32x32x16_f16 v[18:33], v[130:133], v[78:81], v[18:33]
	v_and_b32_e32 v98, 0x1c0, v0
	v_and_b32_e32 v67, 0xc0, v0
	v_lshlrev_b32_e32 v74, 2, v98
	v_mov_b32_e32 v75, v71
	s_movk_i32 s0, 0xfc00
	s_movk_i32 s3, 0x100
	v_lshlrev_b32_e32 v68, 2, v67
	v_mov_b32_e32 v69, v71
	v_lshl_add_u64 v[74:75], s[4:5], 0, v[74:75]
	s_mov_b32 s1, -1
	v_lshl_add_u64 v[68:69], s[10:11], 0, v[68:69]
	v_lshl_add_u64 v[74:75], v[74:75], 0, s[0:1]
	v_mov_b32_e32 v67, 0x3ed96d27
	v_cmp_gt_u32_e32 vcc, s3, v0
	s_barrier
	s_nop 0
	v_cndmask_b32_e32 v72, 1.0, v67, vcc
	v_cndmask_b32_e32 v69, v75, v69, vcc
	v_cndmask_b32_e32 v68, v74, v68, vcc
	v_mov_b32_e32 v67, v71
	v_lshl_add_u64 v[74:75], v[68:69], 0, v[66:67]
	global_load_dwordx4 v[66:69], v[74:75], off
	global_load_dwordx4 v[78:81], v[74:75], off offset:32
	global_load_dwordx4 v[82:85], v[74:75], off offset:64
	global_load_dwordx4 v[86:89], v[74:75], off offset:96
	global_load_dwordx4 v[90:93], v[74:75], off offset:128
	global_load_dwordx4 v[94:97], v[74:75], off offset:160
	s_movk_i32 s0, 0x90
	v_mad_u32_u24 v71, v98, s0, 0
	global_load_dwordx4 v[98:101], v[74:75], off offset:192
	global_load_dwordx4 v[102:105], v[74:75], off offset:224
	v_lshlrev_b32_e32 v77, 3, v77
	v_mul_u32_u24_e32 v1, 0x90, v1
	v_add3_u32 v77, v71, v77, v1
	s_movk_i32 s0, 0xff
	v_add_u32_e32 v106, 0x1000, v77
	v_cmp_lt_u32_e64 s[0:1], s0, v0
	s_lshr_b32 s3, s2, 3
	s_and_b32 s3, s3, 0x3ffc
	s_lshl_b32 s2, s2, 13
	s_and_b32 s2, s2, 0x3e000
	s_waitcnt vmcnt(7)
	v_pk_add_f32 v[50:51], v[66:67], v[50:51]
	v_pk_add_f32 v[52:53], v[68:69], v[52:53]
	s_waitcnt vmcnt(6)
	v_pk_add_f32 v[54:55], v[78:79], v[54:55]
	v_pk_add_f32 v[56:57], v[80:81], v[56:57]
	s_waitcnt vmcnt(3)
	v_pk_add_f32 v[18:19], v[90:91], v[18:19]
	v_pk_add_f32 v[20:21], v[92:93], v[20:21]
	v_pk_add_f32 v[2:3], v[90:91], v[2:3]
	v_pk_add_f32 v[4:5], v[92:93], v[4:5]
	v_pk_mul_f32 v[18:19], v[72:73], v[18:19] op_sel_hi:[0,1]
	v_pk_mul_f32 v[20:21], v[72:73], v[20:21] op_sel_hi:[0,1]
	v_pk_mul_f32 v[2:3], v[72:73], v[2:3] op_sel_hi:[0,1]
	v_pk_mul_f32 v[4:5], v[72:73], v[4:5] op_sel_hi:[0,1]
	v_cvt_pk_f16_f32 v18, v18, v19
	v_cvt_pk_f16_f32 v19, v20, v21
	v_cvt_pk_f16_f32 v2, v2, v3
	v_cvt_pk_f16_f32 v3, v4, v5
	s_waitcnt vmcnt(2)
	v_pk_add_f32 v[4:5], v[94:95], v[22:23]
	v_pk_add_f32 v[20:21], v[96:97], v[24:25]
	v_pk_add_f32 v[58:59], v[82:83], v[58:59]
	v_pk_add_f32 v[60:61], v[84:85], v[60:61]
	v_pk_add_f32 v[62:63], v[86:87], v[62:63]
	v_pk_add_f32 v[64:65], v[88:89], v[64:65]
	v_pk_add_f32 v[34:35], v[66:67], v[34:35]
	v_pk_add_f32 v[36:37], v[68:69], v[36:37]
	v_pk_add_f32 v[38:39], v[78:79], v[38:39]
	v_pk_add_f32 v[40:41], v[80:81], v[40:41]
	v_pk_mul_f32 v[50:51], v[72:73], v[50:51] op_sel_hi:[0,1]
	v_pk_mul_f32 v[52:53], v[72:73], v[52:53] op_sel_hi:[0,1]
	v_pk_mul_f32 v[54:55], v[72:73], v[54:55] op_sel_hi:[0,1]
	v_pk_mul_f32 v[56:57], v[72:73], v[56:57] op_sel_hi:[0,1]
	v_pk_mul_f32 v[4:5], v[72:73], v[4:5] op_sel_hi:[0,1]
	v_pk_mul_f32 v[20:21], v[72:73], v[20:21] op_sel_hi:[0,1]
	v_pk_mul_f32 v[34:35], v[72:73], v[34:35] op_sel_hi:[0,1]
	v_pk_mul_f32 v[36:37], v[72:73], v[36:37] op_sel_hi:[0,1]
	v_pk_mul_f32 v[38:39], v[72:73], v[38:39] op_sel_hi:[0,1]
	v_pk_mul_f32 v[40:41], v[72:73], v[40:41] op_sel_hi:[0,1]
	v_pk_mul_f32 v[58:59], v[72:73], v[58:59] op_sel_hi:[0,1]
	v_pk_mul_f32 v[60:61], v[72:73], v[60:61] op_sel_hi:[0,1]
	v_pk_mul_f32 v[62:63], v[72:73], v[62:63] op_sel_hi:[0,1]
	v_pk_mul_f32 v[64:65], v[72:73], v[64:65] op_sel_hi:[0,1]
	v_cvt_pk_f16_f32 v50, v50, v51
	v_cvt_pk_f16_f32 v51, v52, v53
	v_cvt_pk_f16_f32 v52, v54, v55
	v_cvt_pk_f16_f32 v53, v56, v57
	v_cvt_pk_f16_f32 v4, v4, v5
	v_cvt_pk_f16_f32 v5, v20, v21
	v_cvt_pk_f16_f32 v34, v34, v35
	v_cvt_pk_f16_f32 v35, v36, v37
	v_cvt_pk_f16_f32 v36, v38, v39
	v_cvt_pk_f16_f32 v37, v40, v41
	v_cvt_pk_f16_f32 v38, v58, v59
	v_cvt_pk_f16_f32 v39, v60, v61
	v_cvt_pk_f16_f32 v40, v62, v63
	v_cvt_pk_f16_f32 v41, v64, v65
	ds_write2_b64 v77, v[50:51], v[52:53] offset1:2
	ds_write2_b64 v106, v[34:35], v[36:37] offset0:64 offset1:66
	ds_write2_b64 v77, v[38:39], v[40:41] offset0:4 offset1:6
	ds_write2_b64 v77, v[18:19], v[4:5] offset0:8 offset1:10
	v_pk_add_f32 v[0:1], v[94:95], v[6:7]
	v_pk_add_f32 v[4:5], v[96:97], v[8:9]
	v_pk_mul_f32 v[0:1], v[72:73], v[0:1] op_sel_hi:[0,1]
	v_pk_mul_f32 v[4:5], v[72:73], v[4:5] op_sel_hi:[0,1]
	v_cvt_pk_f16_f32 v0, v0, v1
	v_cvt_pk_f16_f32 v1, v4, v5
	ds_write2_b64 v106, v[2:3], v[0:1] offset0:72 offset1:74
	s_waitcnt vmcnt(1)
	v_pk_add_f32 v[0:1], v[98:99], v[26:27]
	v_pk_add_f32 v[2:3], v[100:101], v[28:29]
	v_pk_mul_f32 v[0:1], v[72:73], v[0:1] op_sel_hi:[0,1]
	v_pk_mul_f32 v[2:3], v[72:73], v[2:3] op_sel_hi:[0,1]
	v_cvt_pk_f16_f32 v0, v0, v1
	v_cvt_pk_f16_f32 v1, v2, v3
	v_pk_add_f32 v[2:3], v[98:99], v[10:11]
	v_pk_add_f32 v[4:5], v[100:101], v[12:13]
	v_pk_mul_f32 v[2:3], v[72:73], v[2:3] op_sel_hi:[0,1]
	v_pk_mul_f32 v[4:5], v[72:73], v[4:5] op_sel_hi:[0,1]
	v_cvt_pk_f16_f32 v2, v2, v3
	v_cvt_pk_f16_f32 v3, v4, v5
	s_waitcnt vmcnt(0)
	v_pk_add_f32 v[4:5], v[102:103], v[30:31]
	v_pk_add_f32 v[6:7], v[104:105], v[32:33]
	v_pk_mul_f32 v[4:5], v[72:73], v[4:5] op_sel_hi:[0,1]
	v_pk_mul_f32 v[6:7], v[72:73], v[6:7] op_sel_hi:[0,1]
	v_cvt_pk_f16_f32 v4, v4, v5
	v_cvt_pk_f16_f32 v5, v6, v7
	ds_write2_b64 v77, v[0:1], v[4:5] offset0:12 offset1:14
	v_pk_add_f32 v[0:1], v[102:103], v[14:15]
	v_pk_add_f32 v[4:5], v[104:105], v[16:17]
	v_pk_mul_f32 v[0:1], v[72:73], v[0:1] op_sel_hi:[0,1]
	v_pk_mul_f32 v[4:5], v[72:73], v[4:5] op_sel_hi:[0,1]
	v_cvt_pk_f16_f32 v0, v0, v1
	v_cvt_pk_f16_f32 v1, v4, v5
	ds_write2_b64 v106, v[2:3], v[0:1] offset0:76 offset1:78
	v_mov_b32_e32 v0, s12
	v_mov_b32_e32 v1, s6
	v_pk_add_f32 v[42:43], v[82:83], v[42:43]
	v_pk_add_f32 v[44:45], v[84:85], v[44:45]
	v_pk_add_f32 v[46:47], v[86:87], v[46:47]
	v_pk_add_f32 v[48:49], v[88:89], v[48:49]
	v_cndmask_b32_e32 v0, v0, v1, vcc
	v_mov_b32_e32 v1, s13
	v_mov_b32_e32 v2, s7
	v_and_or_b32 v4, v76, 3, s3
	v_pk_mul_f32 v[42:43], v[72:73], v[42:43] op_sel_hi:[0,1]
	v_pk_mul_f32 v[44:45], v[72:73], v[44:45] op_sel_hi:[0,1]
	v_pk_mul_f32 v[46:47], v[72:73], v[46:47] op_sel_hi:[0,1]
	v_pk_mul_f32 v[48:49], v[72:73], v[48:49] op_sel_hi:[0,1]
	v_cndmask_b32_e32 v1, v1, v2, vcc
	v_lshl_or_b32 v4, v4, 18, s2
	v_cvt_pk_f16_f32 v42, v42, v43
	v_cvt_pk_f16_f32 v43, v44, v45
	v_cvt_pk_f16_f32 v44, v46, v47
	v_cvt_pk_f16_f32 v45, v48, v49
	v_and_b32_e32 v1, 0xffff, v1
	v_mov_b32_e32 v2, 0x800000
	v_mov_b32_e32 v3, 0x20000
	v_lshl_or_b32 v8, v73, 4, v4
	ds_write2_b64 v106, v[42:43], v[44:45] offset0:68 offset1:70
	s_waitcnt lgkmcnt(0)
	v_readfirstlane_b32 s4, v0
	v_readfirstlane_b32 s5, v1
	v_readfirstlane_b32 s8, v76
	s_mov_b32 s6, 0x800000
	s_mov_b32 s7, 0x20000
	v_add_u32_e32 v10, 0x1000, v8
	v_lshrrev_b32_e32 v4, 2, v73
	v_mul_u32_u24_e32 v4, 0x90, v4
	v_and_b32_e32 v5, 48, v70
	s_movk_i32 s0, 0x90
	s_cmp_lt_u32 s8, 4
	s_cbranch_scc1 .Lmy_proj_qk
	v_add3_u32 v9, v71, v4, v5
	ds_read_b128 v[12:15], v9
	ds_read_b128 v[16:19], v9 offset:2304
	ds_read_b128 v[20:23], v9 offset:4608
	ds_read_b128 v[24:27], v9 offset:6912
	ds_read_b128 v[28:31], v9 offset:64
	ds_read_b128 v[32:35], v9 offset:2368
	ds_read_b128 v[36:39], v9 offset:4672
	ds_read_b128 v[40:43], v9 offset:6976
	s_waitcnt lgkmcnt(7)
	buffer_store_dwordx4 v[12:15], v8, s[4:7], 0 offen sc1
	s_waitcnt lgkmcnt(6)
	buffer_store_dwordx4 v[16:19], v8, s[4:7], 0 offen offset:1024 sc1
	s_waitcnt lgkmcnt(5)
	buffer_store_dwordx4 v[20:23], v8, s[4:7], 0 offen offset:2048 sc1
	s_waitcnt lgkmcnt(4)
	buffer_store_dwordx4 v[24:27], v8, s[4:7], 0 offen offset:3072 sc1
	s_waitcnt lgkmcnt(3)
	buffer_store_dwordx4 v[28:31], v10, s[4:7], 0 offen sc1
	s_waitcnt lgkmcnt(2)
	buffer_store_dwordx4 v[32:35], v10, s[4:7], 0 offen offset:1024 sc1
	s_waitcnt lgkmcnt(1)
	buffer_store_dwordx4 v[36:39], v10, s[4:7], 0 offen offset:2048 sc1
	s_waitcnt lgkmcnt(0)
	buffer_store_dwordx4 v[40:43], v10, s[4:7], 0 offen offset:3072 sc1
	s_endpgm
